# v13 with 8 L2-prefetch helpers per sequence (WGs 16..79), lead 16 chunks
# speedup vs baseline: 1.0060x; 1.0060x over previous
; #define LAS __attribute__((address_space(3)))
; DI int tidx() { int t = threadIdx.x & 255; asm volatile("" : "+v"(t)); return t; }
; DI void phase_mixer(const Params& p, int bid, int nb, char* lds, char* ctl, char* ldsf) {
;   const int vb = threadIdx.x >> 8, lane = tidx() & 63;
;   if (bid < 32) { if (vb == 0) gdn_scan_seq(p, bid >> 1, ldsf); else { __syncthreads(); for (int k = 0; k < 128; ++k) { __builtin_amdgcn_s_barrier(); asm volatile("" ::: "memory"); } __syncthreads(); } }
;   unsigned* ctr = (unsigned*)(p.ws + WS_CTL);
;   volatile LAS int* slot = (volatile LAS int*)(ctl + 16 + 4 * vb);
.LBB0_1226:
.LBB0_1227:
	s_or_b64 exec, exec, s[0:1]
	v_readlane_b32 s2, v250, 0
	v_readfirstlane_b32 s3, v207
	s_nop 3
	s_sub_u32 s14, s2, 16
	s_cmp_lt_u32 s14, 64
	s_cbranch_scc0 .Lpf_done
	s_and_b32 s15, s3, 0xff
	s_cmp_eq_u32 s15, 0
	s_cbranch_scc0 .Lpf_done
	s_lshr_b32 s24, s14, 3
	s_and_b32 s14, s14, 7
	s_lshr_b32 s15, s3, 8
	s_lshl_b32 s15, s15, 3
	s_add_u32 s14, s14, s15
	s_lshl_b32 s15, s14, 21
	s_lshl_b32 s3, s24, 14
	s_add_u32 s15, s15, s3
	s_add_u32 s16, s84, s15
	s_addc_u32 s17, s85, 0
	s_add_u32 s18, s16, 0x1c000000
	s_addc_u32 s19, s17, 0
	s_add_u32 s16, s16, 0x1e000000
	s_addc_u32 s17, s17, 0
	s_add_u32 s22, s66, s15
	s_addc_u32 s23, s67, 0
	s_add_u32 s22, s22, 0x2000000
	s_addc_u32 s23, s23, 0
	s_lshl_b32 s15, s14, 6
	s_add_u32 s2, s84, s15
	s_addc_u32 s3, s85, 0
	s_add_u32 s2, s2, 0xc00
	s_addc_u32 s3, s3, 0
	v_mbcnt_lo_u32_b32 v0, -1, 0
	v_mbcnt_hi_u32_b32 v0, -1, v0
	v_lshlrev_b32_e32 v0, 7, v0
	v_add_u32_e32 v111, 0x2000, v0
	v_mov_b32_e32 v1, 0
	s_mov_b32 s14, s24
	s_mov_b32 s24, 0
.Lpf_loop:
	s_cmp_lt_u32 s14, 16
	s_cbranch_scc1 .Lpf_go
.Lpf_poll:
	global_load_dword v2, v1, s[2:3] sc1
	s_waitcnt vmcnt(0)
	v_readfirstlane_b32 s15, v2
	s_add_u32 s24, s24, 1
	s_add_u32 s15, s15, 16
	s_cmp_ge_u32 s15, s14
	s_cbranch_scc1 .Lpf_go
	s_cmp_gt_u32 s24, 0x1000
	s_cbranch_scc1 .Lpf_end
	s_sleep 8
	s_branch .Lpf_poll
.Lpf_go:
	global_load_dword v2, v0, s[16:17]
	global_load_dword v2, v111, s[16:17]
	global_load_dword v2, v0, s[22:23]
	global_load_dword v2, v111, s[22:23]
	global_load_dword v2, v0, s[18:19]
	global_load_dword v2, v111, s[18:19]
	s_add_u32 s16, s16, 0x20000
	s_addc_u32 s17, s17, 0
	s_add_u32 s22, s22, 0x20000
	s_addc_u32 s23, s23, 0
	s_add_u32 s18, s18, 0x20000
	s_addc_u32 s19, s19, 0
	s_add_u32 s14, s14, 8
	s_cmp_lt_u32 s14, 0x80
	s_cbranch_scc1 .Lpf_loop
